# P7: C=0 first MFMAs instead of zero-init, counted vmcnt for gather-index wait and first-iteration waits; P9: next-token slot broadcast deferred
# speedup vs baseline: 1.0153x; 1.0025x over previous
; #define PG8_STAGE(bufoff, gbase, voff) do { if constexpr (!(Sched::CRIP & 2)) _Pragma("unroll") for (int _i = 0; _i < 2; ++_i) { unsigned _o = (voff)[_i]; asm volatile("" : "+v"(_o)); \
;         __builtin_amdgcn_global_load_lds((const unsigned*)((const char*)(gbase) + _o), (LAS unsigned*)(lds + (bufoff) + ldsw + _i * 8192), 16, 0, 0); } } while (0)
; #define PG8_WAIT_V(n) asm volatile("s_waitcnt vmcnt(" #n ")" ::: "memory")
; #define PG8_BAR __builtin_amdgcn_s_barrier()
; template <class Epi, class Sched>
; __device__ __forceinline__ void gemm_phase(LAS unsigned char* lds, const Sched& S, const Epi& E) {
;     ...
;     int crot = KROT(cur.pm, cur.pn);
;     PG8_STAGE(PG8_SB(0, 0), cB + PG8_KT(crot, 0), voffB); PG8_STAGE(PG8_SB(0, 1), cB + hstep + PG8_KT(crot, 0), voffB); PG8_STAGE(PG8_SA(0, 0), cA + PG8_KT(crot, 0), vA[0]); PG8_STAGE(PG8_SA(0, 1), cA + PG8_KT(crot, 0), vA[1]);
;     if (wr == 1) PG8_BAR;
;     PG8_WAIT_V(2); PG8_BAR;
;     PG8_STAGE(PG8_SB(1, 0), cB + PG8_KT(crot, 1), voffB); PG8_STAGE(PG8_SA(1, 0), cA + PG8_KT(crot, 1), vA[0]); PG8_STAGE(PG8_SB(1, 1), cB + hstep + PG8_KT(crot, 1), voffB);
;     PG8_WAIT_V(6); PG8_BAR;
.LBB0_724:
	s_add_u32 s12, s88, 0x3a800000
	s_addc_u32 s13, s89, 0
	s_lshl_b32 s2, s2, 12
	s_addk_i32 s7, 0x80
	s_lshl_b32 s14, s3, 13
	s_and_b32 s15, s2, 0x3000
	s_and_b32 s7, s7, 0x780
	s_add_u32 s2, s28, s7
	v_mov_b32_e32 v2, v1
	s_waitcnt vmcnt(2)
	s_barrier
	s_addc_u32 s3, s29, 0
	s_add_i32 m0, s39, 0x18000
	v_lshlrev_b32_e32 v3, 6, v0
	global_load_lds_dwordx4 v2, s[2:3]
	v_mov_b32_e32 v2, v190
	s_add_i32 m0, s39, 0x1a000
	v_lshlrev_b32_e32 v5, 2, v0
	global_load_lds_dwordx4 v2, s[2:3]
	s_add_u32 s2, s58, s7
	s_addc_u32 s3, s59, 0
	v_mov_b32_e32 v2, v192
	s_add_i32 s70, s39, 0x8000
	s_mov_b32 m0, s70
	s_add_i32 s71, s39, 0xa000
	global_load_lds_dwordx4 v2, s[2:3]
	v_mov_b32_e32 v2, v194
	s_mov_b32 m0, s71
	v_and_b32_e32 v3, 0x3c0, v3
	global_load_lds_dwordx4 v2, s[2:3]
	s_add_u32 s2, s4, s7
	v_mov_b32_e32 v2, v1
	s_addc_u32 s3, s5, 0
	s_add_i32 m0, s39, 0x1c000
	v_and_b32_e32 v6, 32, v5
	global_load_lds_dwordx4 v2, s[2:3]
	v_mov_b32_e32 v2, v190
	s_add_i32 m0, s39, 0x1e000
	s_cmpk_lt_u32 s6, 0x100
	global_load_lds_dwordx4 v2, s[2:3]
	v_and_b32_e32 v2, 48, v0
	v_or_b32_e32 v4, v3, v2
	v_bitop3_b32 v2, v3, v6, v2 bitop3:0x36
	v_bitop3_b32 v3, s14, v4, v6 bitop3:0xf6
	v_or_b32_e32 v196, s15, v2
	s_cselect_b64 s[14:15], -1, 0
	s_add_i32 s3, 0, 0x27d04
	v_writelane_b32 v255, s3, 55
	s_add_i32 s3, 0, 0x27d4c
	v_writelane_b32 v255, s3, 56
	s_add_i32 s3, 0, 0x27d54
	v_writelane_b32 v255, s3, 57
	s_add_i32 s3, 0, 0x27d5c
	v_writelane_b32 v255, s3, 58
	s_add_i32 s3, 0, 0x27d64
	s_waitcnt vmcnt(0)
	v_writelane_b32 v255, s3, 59
	s_add_i32 s3, 0, 0x27d6c
	s_mov_b32 s4, 0
	s_add_i32 s2, 0, 0x27d80
	v_writelane_b32 v255, s3, 60
	s_add_i32 s3, 0, 0x27d74
	v_mov_b32_e32 v187, 0
	v_add_u32_e32 v197, s60, v5
	s_ashr_i32 s96, s96, 31
	s_add_i32 s9, 0, 0x27d0c
	s_add_i32 s8, 0, 0x27d14
	s_add_i32 s17, 0, 0x27d1c
	s_add_i32 s50, 0, 0x27d24
	s_add_i32 s10, 0, 0x27d2c
	s_add_i32 s11, 0, 0x27d34
	s_add_i32 s56, 0, 0x27d3c
	s_add_i32 s57, 0, 0x27d44
	v_writelane_b32 v255, s3, 61
	s_add_i32 s91, 0, 0x27d7c
	v_lshlrev_b32_e32 v198, 2, v0
	s_add_i32 s92, 0, 0x10000
	s_add_i32 s93, 0, 0x14000
	s_mov_b32 s5, s4
	s_mov_b32 s6, s4
	s_mov_b32 s7, s4
	s_mov_b32 s16, 0xc01d265f
	s_mov_b32 s94, 0xc0e00000
	v_mov_b32_e32 v199, s2
	v_add_u32_e32 v200, 0, v3
	v_mov_b32_e32 v201, 1
	v_mov_b32_e32 v42, 0xba1d265f
	v_mov_b32_e32 v46, 0x39800000
	v_mov_b32_e32 v202, 0x40e00000
	v_mov_b32_e32 v188, 0x3fd083aa
	s_mov_b32 s95, s4
	s_mov_b64 s[24:25], s[28:29]
	s_barrier
	s_branch .LBB0_727

; #define PG8_STAGE(bufoff, gbase, voff) do { if constexpr (!(Sched::CRIP & 2)) _Pragma("unroll") for (int _i = 0; _i < 2; ++_i) { unsigned _o = (voff)[_i]; asm volatile("" : "+v"(_o)); \
;         __builtin_amdgcn_global_load_lds((const unsigned*)((const char*)(gbase) + _o), (LAS unsigned*)(lds + (bufoff) + ldsw + _i * 8192), 16, 0, 0); } } while (0)
; #define PG8_LDA(dst, b, h) do { if constexpr (!(Sched::CRIP & 4)) _Pragma("unroll") for (int m = 0; m < 4; ++m) dst[m] = PG8_CAT(*(const LAS i32x4*)(lds + PG8_SA(b, h) + aoff + m * 2048), *(const LAS i32x4*)(lds + PG8_SA(b, h) + aoff + m * 2048 + 1024)); } while (0)
; #define PG8_LDB(dst, b, h) do { if constexpr (!(Sched::CRIP & 4)) _Pragma("unroll") for (int n = 0; n < 2; ++n) dst[n] = PG8_CAT(*(const LAS i32x4*)(lds + PG8_SB(b, h) + boff + n * 2048), *(const LAS i32x4*)(lds + PG8_SB(b, h) + boff + n * 2048 + 1024)); } while (0)
; #define PG8_WAIT_V(n) asm volatile("s_waitcnt vmcnt(" #n ")" ::: "memory")
; #define PG8_WAIT_L(n) asm volatile("s_waitcnt lgkmcnt(" #n ")" ::: "memory")
; #define PG8_BAR __builtin_amdgcn_s_barrier()
; #define PG8_SCHED __builtin_amdgcn_sched_barrier(0)
; template <class Epi, class Sched>
; __device__ __forceinline__ void gemm_phase(LAS unsigned char* lds, const Sched& S, const Epi& E) {
;     ...
;             if constexpr (Sched::GATHER) { if (t == 0 && has_next && tid < 256) gi = nxt.aidx[tid]; }
;             PG8_LDB(B0, 0, 0); PG8_LDB(B1, 0, 1); PG8_SCHED; PG8_LDA(At, 0, 0); PG8_STAGE(PG8_SA(1, 1), a1, vA[1]);
;             PG8_WAIT_V(8); PG8_WAIT_L(0); PG8_BAR; PG8_MMA(0, 0, At, B0); PG8_MMA(0, 1, At, B1); PG8_BAR2; PG8_SCHED;
;             if constexpr (Sched::GATHER) { if (last && has_next) {
;                 int tz = threadIdx.x; asm volatile("" : "+v"(tz));
; #pragma unroll
;                 for (int i = 0; i < 2; ++i) { int R, C; stage_rc(tz * 16 + i * 8192, R, C);
; #pragma unroll
;                     for (int h = 0; h < 2; ++h) vA[h][i] = (unsigned)(lidx[h * HALF + R] * RP + C * 2); } } }
;             PG8_LDA(At, 0, 1); PG8_STAGE(PG8_SB(0, 0), b2, voffB); PG8_STAGE(PG8_SB(0, 1), b2 + hstep, voffB); PG8_STAGE(PG8_SA(0, 0), a2, vA[0]);
;             PG8_WAIT_V(8); PG8_WAIT_L(0); PG8_BAR; PG8_MMA(1, 0, At, B0); PG8_MMA(1, 1, At, B1); PG8_BAR2; PG8_SCHED;
.LBB0_731:
	s_or_b64 exec, exec, s[34:35]
	s_lshl_b32 s18, s19, 7
	s_add_i32 s21, s18, 0x80
	s_and_b32 s21, s21, 0x780
	s_add_u32 s46, s58, s21
	s_addc_u32 s47, s59, 0
	s_add_i32 s21, s18, 0x100
	s_and_b32 s21, s21, 0x780
	v_add_u32_e32 v3, s92, v196
	s_add_u32 s40, s58, s21
	ds_read_b128 v[4:7], v3
	ds_read_b128 v[8:11], v3 offset:1024
	ds_read_b128 v[12:15], v3 offset:2048
	ds_read_b128 v[16:19], v3 offset:3072
	v_add_u32_e32 v3, s93, v196
	s_addc_u32 s41, s59, 0
	ds_read_b128 v[20:23], v3
	ds_read_b128 v[24:27], v3 offset:1024
	ds_read_b128 v[204:207], v3 offset:2048
	ds_read_b128 v[208:211], v3 offset:3072
	s_add_u32 s42, s28, s21
	s_addc_u32 s43, s29, 0
	s_add_i32 s21, s18, 0x180
	s_and_b32 s18, s21, 0x780
	s_add_u32 s34, s58, s18
	s_addc_u32 s35, s59, 0
	s_add_u32 s36, s28, s18
	s_addc_u32 s37, s29, 0
	v_mov_b32_e32 v3, v193
	s_add_i32 s27, s39, 0xc000
	ds_read_b128 v[48:51], v200
	ds_read_b128 v[52:55], v200 offset:1024
	ds_read_b128 v[56:59], v200 offset:2048
	ds_read_b128 v[60:63], v200 offset:3072
	ds_read_b128 v[64:67], v200 offset:4096
	ds_read_b128 v[68:71], v200 offset:5120
	ds_read_b128 v[82:85], v200 offset:6144
	ds_read_b128 v[86:89], v200 offset:7168
	s_mov_b32 m0, s27
	s_add_i32 s62, s39, 0xe000
	global_load_lds_dwordx4 v3, s[46:47]
	v_mov_b32_e32 v3, v195
	s_mov_b32 m0, s62
	s_nop 0
	global_load_lds_dwordx4 v3, s[46:47]
	s_waitcnt vmcnt(16)
	s_waitcnt lgkmcnt(0)
	s_barrier
	s_setprio 1
	s_waitcnt lgkmcnt(0)
	s_nop 1
	v_mfma_scale_f32_16x16x128_f8f6f4 v[178:181], v[4:11], v[48:55], 0, v191, v191 op_sel_hi:[0,0,0]
	v_mfma_scale_f32_16x16x128_f8f6f4 v[170:173], v[12:19], v[48:55], 0, v191, v191 op_sel_hi:[0,0,0]
	v_mfma_scale_f32_16x16x128_f8f6f4 v[162:165], v[4:11], v[56:63], 0, v191, v191 op_sel_hi:[0,0,0]
	v_mfma_scale_f32_16x16x128_f8f6f4 v[154:157], v[12:19], v[56:63], 0, v191, v191 op_sel_hi:[0,0,0]
	v_mfma_scale_f32_16x16x128_f8f6f4 v[146:149], v[4:11], v[64:71], 0, v191, v191 op_sel_hi:[0,0,0]
	v_mfma_scale_f32_16x16x128_f8f6f4 v[138:141], v[12:19], v[64:71], 0, v191, v191 op_sel_hi:[0,0,0]
	v_mfma_scale_f32_16x16x128_f8f6f4 v[130:133], v[4:11], v[82:89], 0, v191, v191 op_sel_hi:[0,0,0]
	v_mfma_scale_f32_16x16x128_f8f6f4 v[122:125], v[12:19], v[82:89], 0, v191, v191 op_sel_hi:[0,0,0]
	s_setprio 0
	s_setprio 1
	s_nop 1
	v_mfma_scale_f32_16x16x128_f8f6f4 v[182:185], v[20:27], v[48:55], 0, v191, v191 op_sel_hi:[0,0,0]
	v_mfma_scale_f32_16x16x128_f8f6f4 v[174:177], v[204:211], v[48:55], 0, v191, v191 op_sel_hi:[0,0,0]
	v_mfma_scale_f32_16x16x128_f8f6f4 v[166:169], v[20:27], v[56:63], 0, v191, v191 op_sel_hi:[0,0,0]
	v_mfma_scale_f32_16x16x128_f8f6f4 v[158:161], v[204:211], v[56:63], 0, v191, v191 op_sel_hi:[0,0,0]
	v_mfma_scale_f32_16x16x128_f8f6f4 v[150:153], v[20:27], v[64:71], 0, v191, v191 op_sel_hi:[0,0,0]
	v_mfma_scale_f32_16x16x128_f8f6f4 v[142:145], v[204:211], v[64:71], 0, v191, v191 op_sel_hi:[0,0,0]
	v_mfma_scale_f32_16x16x128_f8f6f4 v[134:137], v[20:27], v[82:89], 0, v191, v191 op_sel_hi:[0,0,0]
	v_mfma_scale_f32_16x16x128_f8f6f4 v[126:129], v[204:211], v[82:89], 0, v191, v191 op_sel_hi:[0,0,0]
	s_setprio 0
	s_barrier
	v_mov_b32_e32 v3, v1
	s_add_i32 s18, s92, s61
	ds_read_b128 v[218:221], v200 offset:23552
	ds_read_b128 v[214:217], v200 offset:22528
	ds_read_b128 v[226:229], v200 offset:21504
	ds_read_b128 v[222:225], v200 offset:20480
	ds_read_b128 v[234:237], v200 offset:19456
	ds_read_b128 v[230:233], v200 offset:18432
	ds_read_b128 v[242:245], v200 offset:17408
	ds_read_b128 v[238:241], v200 offset:16384
	s_mov_b32 m0, s18
	s_nop 0
	global_load_lds_dwordx4 v3, s[42:43]
	v_mov_b32_e32 v3, v190
	s_add_i32 m0, s18, 0x2000
	s_nop 0
	global_load_lds_dwordx4 v3, s[42:43]
	s_add_u32 s42, s42, 0x40000
	s_addc_u32 s43, s43, 0
	v_mov_b32_e32 v3, v1
	s_add_i32 s18, s93, s61
	s_mov_b32 m0, s18
	s_nop 0
	global_load_lds_dwordx4 v3, s[42:43]
	v_mov_b32_e32 v3, v190
	s_add_i32 m0, s18, 0x2000
	s_nop 0
	global_load_lds_dwordx4 v3, s[42:43]
	v_mov_b32_e32 v3, v192
	s_mov_b32 m0, s39
	s_nop 0
	global_load_lds_dwordx4 v3, s[40:41]
	v_mov_b32_e32 v3, v194
	s_mov_b32 m0, s67
	s_nop 0
	global_load_lds_dwordx4 v3, s[40:41]
	s_waitcnt vmcnt(16)
	s_waitcnt lgkmcnt(0)
	s_barrier
	s_setprio 1
	s_waitcnt lgkmcnt(0)
	s_nop 1
	v_mfma_scale_f32_16x16x128_f8f6f4 v[118:121], v[4:11], v[238:245], 0, v191, v191 op_sel_hi:[0,0,0]
	v_mfma_scale_f32_16x16x128_f8f6f4 v[110:113], v[12:19], v[238:245], 0, v191, v191 op_sel_hi:[0,0,0]
	v_mfma_scale_f32_16x16x128_f8f6f4 v[98:101], v[4:11], v[230:237], 0, v191, v191 op_sel_hi:[0,0,0]
	v_mfma_scale_f32_16x16x128_f8f6f4 v[90:93], v[12:19], v[230:237], 0, v191, v191 op_sel_hi:[0,0,0]
	v_mfma_scale_f32_16x16x128_f8f6f4 v[82:85], v[4:11], v[222:229], 0, v191, v191 op_sel_hi:[0,0,0]
	v_mfma_scale_f32_16x16x128_f8f6f4 v[66:69], v[12:19], v[222:229], 0, v191, v191 op_sel_hi:[0,0,0]
	v_mfma_scale_f32_16x16x128_f8f6f4 v[58:61], v[4:11], v[214:221], 0, v191, v191 op_sel_hi:[0,0,0]
	v_mfma_scale_f32_16x16x128_f8f6f4 v[50:53], v[12:19], v[214:221], 0, v191, v191 op_sel_hi:[0,0,0]
	s_setprio 0
	s_setprio 1
	s_nop 1
	v_mfma_scale_f32_16x16x128_f8f6f4 v[106:109], v[20:27], v[238:245], 0, v191, v191 op_sel_hi:[0,0,0]
	v_mfma_scale_f32_16x16x128_f8f6f4 v[114:117], v[204:211], v[238:245], 0, v191, v191 op_sel_hi:[0,0,0]
	v_mfma_scale_f32_16x16x128_f8f6f4 v[102:105], v[20:27], v[230:237], 0, v191, v191 op_sel_hi:[0,0,0]
	v_mfma_scale_f32_16x16x128_f8f6f4 v[94:97], v[204:211], v[230:237], 0, v191, v191 op_sel_hi:[0,0,0]
	v_mfma_scale_f32_16x16x128_f8f6f4 v[86:89], v[20:27], v[222:229], 0, v191, v191 op_sel_hi:[0,0,0]
	v_mfma_scale_f32_16x16x128_f8f6f4 v[70:73], v[204:211], v[222:229], 0, v191, v191 op_sel_hi:[0,0,0]
	v_mfma_scale_f32_16x16x128_f8f6f4 v[62:65], v[20:27], v[214:221], 0, v191, v191 op_sel_hi:[0,0,0]
	v_mfma_scale_f32_16x16x128_f8f6f4 v[54:57], v[204:211], v[214:221], 0, v191, v191 op_sel_hi:[0,0,0]
	s_setprio 0
	s_barrier
; #define PG8_STAGE(bufoff, gbase, voff) do { if constexpr (!(Sched::CRIP & 2)) _Pragma("unroll") for (int _i = 0; _i < 2; ++_i) { unsigned _o = (voff)[_i]; asm volatile("" : "+v"(_o)); \
;         __builtin_amdgcn_global_load_lds((const unsigned*)((const char*)(gbase) + _o), (LAS unsigned*)(lds + (bufoff) + ldsw + _i * 8192), 16, 0, 0); } } while (0)
; #define PG8_LDA(dst, b, h) do { if constexpr (!(Sched::CRIP & 4)) _Pragma("unroll") for (int m = 0; m < 4; ++m) dst[m] = PG8_CAT(*(const LAS i32x4*)(lds + PG8_SA(b, h) + aoff + m * 2048), *(const LAS i32x4*)(lds + PG8_SA(b, h) + aoff + m * 2048 + 1024)); } while (0)
; #define PG8_LDB(dst, b, h) do { if constexpr (!(Sched::CRIP & 4)) _Pragma("unroll") for (int n = 0; n < 2; ++n) dst[n] = PG8_CAT(*(const LAS i32x4*)(lds + PG8_SB(b, h) + boff + n * 2048), *(const LAS i32x4*)(lds + PG8_SB(b, h) + boff + n * 2048 + 1024)); } while (0)
; #define PG8_WAIT_V(n) asm volatile("s_waitcnt vmcnt(" #n ")" ::: "memory")
; #define PG8_WAIT_L(n) asm volatile("s_waitcnt lgkmcnt(" #n ")" ::: "memory")
; #define PG8_BAR __builtin_amdgcn_s_barrier()
; #define PG8_SCHED __builtin_amdgcn_sched_barrier(0)
; template <class Epi, class Sched>
; __device__ __forceinline__ void gemm_phase(LAS unsigned char* lds, const Sched& S, const Epi& E) {
;     ...
;             PG8_LDB(B0, 1, 0); PG8_LDB(B1, 1, 1); PG8_SCHED; PG8_LDA(At, 1, 0); PG8_STAGE(PG8_SA(0, 1), a2, vA[1]);
;             PG8_WAIT_V(8); PG8_WAIT_L(0); PG8_BAR; PG8_MMA(0, 0, At, B0); PG8_MMA(0, 1, At, B1); PG8_BAR2; PG8_SCHED;
;             PG8_LDA(At, 1, 1); PG8_STAGE(PG8_SB(1, 0), b3, voffB); PG8_STAGE(PG8_SB(1, 1), b3 + hstep, voffB); PG8_STAGE(PG8_SA(1, 0), a3, vA[0]);
;             PG8_WAIT_V(8); PG8_WAIT_L(0); PG8_BAR; PG8_MMA(1, 0, At, B0); PG8_MMA(1, 1, At, B1); PG8_BAR2; PG8_SCHED;
;             if constexpr (Sched::GATHER) { if (t == 0 && has_next && tid < 256) lidx[tid] = (tid < nxt.avalid) ? gi : 0; }
	s_add_i32 s18, 0, 0x18000
	s_add_i32 s42, 0, 0x1c000
	v_add_u32_e32 v43, s18, v196
	v_add_u32_e32 v44, s42, v196
	ds_read_b128 v[4:7], v43
	ds_read_b128 v[8:11], v43 offset:1024
	ds_read_b128 v[12:15], v43 offset:2048
	ds_read_b128 v[16:19], v43 offset:3072
	ds_read_b128 v[20:23], v44
	ds_read_b128 v[24:27], v44 offset:1024
	ds_read_b128 v[204:207], v44 offset:2048
	ds_read_b128 v[208:211], v44 offset:3072
	v_mov_b32_e32 v3, v193
	s_mov_b32 m0, s68
	ds_read_b128 v[214:217], v200 offset:32768
	ds_read_b128 v[218:221], v200 offset:33792
	ds_read_b128 v[222:225], v200 offset:34816
	ds_read_b128 v[226:229], v200 offset:35840
	ds_read_b128 v[230:233], v200 offset:36864
	ds_read_b128 v[234:237], v200 offset:37888
	ds_read_b128 v[238:241], v200 offset:38912
	ds_read_b128 v[242:245], v200 offset:39936
	s_nop 0
	global_load_lds_dwordx4 v3, s[40:41]
	v_mov_b32_e32 v3, v195
	s_mov_b32 m0, s69
	s_nop 0
	global_load_lds_dwordx4 v3, s[40:41]
	s_waitcnt vmcnt(8)
	s_waitcnt lgkmcnt(0)
	s_barrier
	s_setprio 1
	s_waitcnt lgkmcnt(0)
	s_nop 1
	v_mfma_scale_f32_16x16x128_f8f6f4 v[178:181], v[4:11], v[214:221], v[178:181], v191, v191 op_sel_hi:[0,0,0]
	v_mfma_scale_f32_16x16x128_f8f6f4 v[170:173], v[12:19], v[214:221], v[170:173], v191, v191 op_sel_hi:[0,0,0]
	v_mfma_scale_f32_16x16x128_f8f6f4 v[162:165], v[4:11], v[222:229], v[162:165], v191, v191 op_sel_hi:[0,0,0]
	v_mfma_scale_f32_16x16x128_f8f6f4 v[154:157], v[12:19], v[222:229], v[154:157], v191, v191 op_sel_hi:[0,0,0]
	v_mfma_scale_f32_16x16x128_f8f6f4 v[146:149], v[4:11], v[230:237], v[146:149], v191, v191 op_sel_hi:[0,0,0]
	v_mfma_scale_f32_16x16x128_f8f6f4 v[138:141], v[12:19], v[230:237], v[138:141], v191, v191 op_sel_hi:[0,0,0]
	v_mfma_scale_f32_16x16x128_f8f6f4 v[130:133], v[4:11], v[238:245], v[130:133], v191, v191 op_sel_hi:[0,0,0]
	v_mfma_scale_f32_16x16x128_f8f6f4 v[122:125], v[12:19], v[238:245], v[122:125], v191, v191 op_sel_hi:[0,0,0]
	s_setprio 0
	s_setprio 1
	s_nop 1
	v_mfma_scale_f32_16x16x128_f8f6f4 v[182:185], v[20:27], v[214:221], v[182:185], v191, v191 op_sel_hi:[0,0,0]
	v_mfma_scale_f32_16x16x128_f8f6f4 v[174:177], v[204:211], v[214:221], v[174:177], v191, v191 op_sel_hi:[0,0,0]
	v_mfma_scale_f32_16x16x128_f8f6f4 v[166:169], v[20:27], v[222:229], v[166:169], v191, v191 op_sel_hi:[0,0,0]
	v_mfma_scale_f32_16x16x128_f8f6f4 v[158:161], v[204:211], v[222:229], v[158:161], v191, v191 op_sel_hi:[0,0,0]
	v_mfma_scale_f32_16x16x128_f8f6f4 v[150:153], v[20:27], v[230:237], v[150:153], v191, v191 op_sel_hi:[0,0,0]
	v_mfma_scale_f32_16x16x128_f8f6f4 v[142:145], v[204:211], v[230:237], v[142:145], v191, v191 op_sel_hi:[0,0,0]
	v_mfma_scale_f32_16x16x128_f8f6f4 v[134:137], v[20:27], v[238:245], v[134:137], v191, v191 op_sel_hi:[0,0,0]
	v_mfma_scale_f32_16x16x128_f8f6f4 v[126:129], v[204:211], v[238:245], v[126:129], v191, v191 op_sel_hi:[0,0,0]
	s_setprio 0
	s_barrier
	v_mov_b32_e32 v3, v1
	s_add_i32 s40, s18, s61
	ds_read_b128 v[214:217], v200 offset:49152
	ds_read_b128 v[218:221], v200 offset:50176
	ds_read_b128 v[222:225], v200 offset:51200
	ds_read_b128 v[226:229], v200 offset:52224
	ds_read_b128 v[230:233], v200 offset:53248
	ds_read_b128 v[234:237], v200 offset:54272
	ds_read_b128 v[238:241], v200 offset:55296
	ds_read_b128 v[242:245], v200 offset:56320
	s_mov_b32 m0, s40
	s_add_i32 s41, s40, 0x2000
	global_load_lds_dwordx4 v3, s[36:37]
	v_mov_b32_e32 v3, v190
	s_mov_b32 m0, s41
	s_nop 0
	global_load_lds_dwordx4 v3, s[36:37]
	s_add_u32 s36, s36, 0x40000
	s_addc_u32 s37, s37, 0
	v_mov_b32_e32 v3, v1
	s_add_i32 s42, s42, s61
	s_mov_b32 m0, s42
	s_add_i32 s43, s42, 0x2000
	global_load_lds_dwordx4 v3, s[36:37]
	v_mov_b32_e32 v3, v190
	s_mov_b32 m0, s43
	s_nop 0
	global_load_lds_dwordx4 v3, s[36:37]
	v_mov_b32_e32 v3, v192
	s_mov_b32 m0, s70
	s_nop 0
	global_load_lds_dwordx4 v3, s[34:35]
	v_mov_b32_e32 v3, v194
	s_mov_b32 m0, s71
	s_nop 0
	global_load_lds_dwordx4 v3, s[34:35]
	s_waitcnt vmcnt(8)
	s_waitcnt lgkmcnt(0)
	s_barrier
	s_setprio 1
	s_waitcnt lgkmcnt(0)
	s_nop 1
	v_mfma_scale_f32_16x16x128_f8f6f4 v[118:121], v[4:11], v[214:221], v[118:121], v191, v191 op_sel_hi:[0,0,0]
	v_mfma_scale_f32_16x16x128_f8f6f4 v[110:113], v[12:19], v[214:221], v[110:113], v191, v191 op_sel_hi:[0,0,0]
	v_mfma_scale_f32_16x16x128_f8f6f4 v[98:101], v[4:11], v[222:229], v[98:101], v191, v191 op_sel_hi:[0,0,0]
	v_mfma_scale_f32_16x16x128_f8f6f4 v[90:93], v[12:19], v[222:229], v[90:93], v191, v191 op_sel_hi:[0,0,0]
	v_mfma_scale_f32_16x16x128_f8f6f4 v[82:85], v[4:11], v[230:237], v[82:85], v191, v191 op_sel_hi:[0,0,0]
	v_mfma_scale_f32_16x16x128_f8f6f4 v[66:69], v[12:19], v[230:237], v[66:69], v191, v191 op_sel_hi:[0,0,0]
	v_mfma_scale_f32_16x16x128_f8f6f4 v[58:61], v[4:11], v[238:245], v[58:61], v191, v191 op_sel_hi:[0,0,0]
	v_mfma_scale_f32_16x16x128_f8f6f4 v[50:53], v[12:19], v[238:245], v[50:53], v191, v191 op_sel_hi:[0,0,0]
	s_setprio 0
	s_setprio 1
	s_nop 1
	v_mfma_scale_f32_16x16x128_f8f6f4 v[106:109], v[20:27], v[214:221], v[106:109], v191, v191 op_sel_hi:[0,0,0]
	v_mfma_scale_f32_16x16x128_f8f6f4 v[114:117], v[204:211], v[214:221], v[114:117], v191, v191 op_sel_hi:[0,0,0]
	v_mfma_scale_f32_16x16x128_f8f6f4 v[102:105], v[20:27], v[222:229], v[102:105], v191, v191 op_sel_hi:[0,0,0]
	v_mfma_scale_f32_16x16x128_f8f6f4 v[94:97], v[204:211], v[222:229], v[94:97], v191, v191 op_sel_hi:[0,0,0]
	v_mfma_scale_f32_16x16x128_f8f6f4 v[86:89], v[20:27], v[230:237], v[86:89], v191, v191 op_sel_hi:[0,0,0]
	v_mfma_scale_f32_16x16x128_f8f6f4 v[70:73], v[204:211], v[230:237], v[70:73], v191, v191 op_sel_hi:[0,0,0]
	v_mfma_scale_f32_16x16x128_f8f6f4 v[62:65], v[20:27], v[238:245], v[62:65], v191, v191 op_sel_hi:[0,0,0]
	v_mfma_scale_f32_16x16x128_f8f6f4 v[54:57], v[204:211], v[238:245], v[54:57], v191, v191 op_sel_hi:[0,0,0]
	s_setprio 0
	s_barrier
	s_and_saveexec_b64 s[34:35], s[30:31]
	s_cbranch_execz .LBB0_733
	v_cmp_gt_i32_e32 vcc, s90, v0
	s_waitcnt vmcnt(8)
	s_nop 0
	v_cndmask_b32_e32 v2, 0, v2, vcc
	ds_write_b32 v197, v2
.LBB0_733:
	s_or_b64 exec, exec, s[34:35]
	s_and_b32 s18, s44, 15
	s_and_b64 s[30:31], s[2:3], exec
	s_cselect_b32 s19, s18, s19
	s_lshl_b32 s19, s19, 7
	s_add_u32 s45, s24, s19
	s_addc_u32 s46, s25, 0
	s_add_i32 s30, s19, 0x80
	s_and_b32 s47, s30, 0x780
	s_add_u32 s48, s24, s47
	s_addc_u32 s49, s25, 0
	s_mov_b32 s52, 0
	s_waitcnt vmcnt(8)
	s_branch .LBB0_735

; __device__ __forceinline__ void unpack8(const v4u q, float (&d)[8]) { d[0] = bflo(q.x); d[1] = bfhi(q.x); d[2] = bflo(q.y); d[3] = bfhi(q.y); d[4] = bflo(q.z); d[5] = bfhi(q.z); d[6] = bflo(q.w); d[7] = bfhi(q.w); }
; __device__ __forceinline__ void phase_combine(const Params& p, const LAS int* tstart, int gw, int NGW, int lane) {
;     ...
;     for (int m = gw; m < T; m += NGW) {
;         const i32x4v ce = ne, cp = np;
;         if (m + NGW < T) { ne = *(const i32x4v*)(toke + (m + NGW) * 4); np = *(const i32x4v*)(tokp + (m + NGW) * 4); }
;         const unsigned char* yr[4];
; #pragma unroll
;         for (int k = 0; k < 4; ++k) yr[k] = y2 + ((size_t)tstart[ce[k]] * 256 + cp[k]) * D;
;         float* op = p.out + (size_t)m * D; const bf16* xp = (const bf16*)(p.ws + WS_X1) + (size_t)m * D;
; #pragma unroll
;         for (int j = 0; j < 2; ++j) { const int c = (j * 64 + lane) * 16;
;             v4u w[4];
; #pragma unroll
;             for (int k = 0; k < 4; ++k) w[k] = *(const v4u*)(yr[k] + c);
;             f32x4 a[4];
;             { const v4u xa = *(const v4u*)(xp + c), xb = *(const v4u*)(xp + c + 8); float fa[8], fb[8]; unpack8(xa, fa); unpack8(xb, fb);
;               a[0] = (f32x4){fa[0], fa[1], fa[2], fa[3]}; a[1] = (f32x4){fa[4], fa[5], fa[6], fa[7]}; a[2] = (f32x4){fb[0], fb[1], fb[2], fb[3]}; a[3] = (f32x4){fb[4], fb[5], fb[6], fb[7]}; }
; #pragma unroll
;             for (int q = 0; q < 4; ++q) { float s0 = 0.f, s1 = 0.f, s2 = 0.f, s3 = 0.f;
; #pragma unroll
;                 for (int k = 0; k < 4; ++k) { const int wd = (int)(q == 0 ? w[k].x : q == 1 ? w[k].y : q == 2 ? w[k].z : w[k].w);
;                     const f32x2 lo = __builtin_amdgcn_cvt_pk_f32_fp8(wd, false), hi = __builtin_amdgcn_cvt_pk_f32_fp8(wd, true);
;                     s0 += lo.x; s1 += lo.y; s2 += hi.x; s3 += hi.y; }
;                 a[q][0] += s0 * DY; a[q][1] += s1 * DY; a[q][2] += s2 * DY; a[q][3] += s3 * DY;
;                 *(f32x4*)(op + c + 4 * q) = a[q]; }
.LBB0_871:
	v_lshlrev_b32_e32 v4, 2, v4
	v_add_u32_e32 v4, s24, v4
	ds_read_b32 v4, v4
	v_lshlrev_b32_e32 v5, 2, v5
	v_lshlrev_b32_e32 v6, 2, v6
	v_add_u32_e32 v5, s24, v5
	v_add_u32_e32 v14, s24, v6
	v_lshlrev_b32_e32 v6, 2, v7
	v_add_u32_e32 v7, s24, v6
	ds_read_b32 v6, v5
	ds_read_b32 v14, v14
	ds_read_b32 v16, v7
	s_waitcnt lgkmcnt(3)
	v_ashrrev_i32_e32 v5, 31, v4
	s_ashr_i32 s27, s4, 31
	s_mov_b32 s26, s4
	v_lshlrev_b64 v[4:5], 19, v[4:5]
	s_lshl_b64 s[26:27], s[26:27], 11
	v_lshl_add_u64 v[4:5], s[8:9], 0, v[4:5]
	s_waitcnt lgkmcnt(2)
	v_ashrrev_i32_e32 v7, 31, v6
	v_lshl_add_u64 v[18:19], v[4:5], 0, s[26:27]
	s_ashr_i32 s27, s5, 31
	s_mov_b32 s26, s5
	v_lshlrev_b64 v[4:5], 19, v[6:7]
	s_lshl_b64 s[4:5], s[26:27], 11
	v_lshl_add_u64 v[4:5], s[8:9], 0, v[4:5]
	s_waitcnt lgkmcnt(1)
	v_ashrrev_i32_e32 v15, 31, v14
	v_lshl_add_u64 v[20:21], v[4:5], 0, s[4:5]
	s_ashr_i32 s5, s6, 31
	s_mov_b32 s4, s6
	v_lshlrev_b64 v[4:5], 19, v[14:15]
	s_lshl_b64 s[4:5], s[4:5], 11
	v_lshl_add_u64 v[4:5], s[8:9], 0, v[4:5]
	s_waitcnt lgkmcnt(0)
	v_ashrrev_i32_e32 v17, 31, v16
	v_lshl_add_u64 v[22:23], v[4:5], 0, s[4:5]
	s_ashr_i32 s5, s7, 31
	s_mov_b32 s4, s7
	v_lshlrev_b64 v[14:15], 19, v[16:17]
	s_lshl_b64 s[4:5], s[4:5], 11
	v_lshl_add_u64 v[14:15], s[8:9], 0, v[14:15]
	v_lshl_add_u64 v[38:39], v[18:19], 0, v[8:9]
	global_load_dwordx4 v[4:7], v[10:11], off
	v_lshl_add_u64 v[26:27], v[14:15], 0, s[4:5]
	global_load_dwordx4 v[14:17], v[38:39], off
	v_lshl_add_u64 v[40:41], v[20:21], 0, v[8:9]
	global_load_dwordx4 v[18:21], v[40:41], off
	v_lshl_add_u64 v[42:43], v[22:23], 0, v[8:9]
	global_load_dwordx4 v[22:25], v[42:43], off
	v_lshl_add_u64 v[44:45], v[26:27], 0, v[8:9]
	global_load_dwordx4 v[26:29], v[44:45], off
	global_load_dwordx4 v[30:33], v[10:11], off offset:16
	s_add_i32 s16, s16, s23
	s_andn2_b64 vcc, exec, s[18:19]
	s_waitcnt vmcnt(5)
	v_readfirstlane_b32 s4, v84
	v_readfirstlane_b32 s5, v85
	v_readfirstlane_b32 s6, v86
	v_readfirstlane_b32 s7, v87
	v_lshlrev_b32_e32 v34, 16, v4
	v_and_b32_e32 v35, 0xffff0000, v4
	v_lshlrev_b32_e32 v36, 16, v5
	v_and_b32_e32 v37, 0xffff0000, v5
	v_lshlrev_b32_e32 v46, 16, v6
	v_and_b32_e32 v47, 0xffff0000, v6
	v_lshlrev_b32_e32 v48, 16, v7
	v_and_b32_e32 v49, 0xffff0000, v7
	s_waitcnt vmcnt(4)
	v_cvt_pk_f32_fp8_e32 v[4:5], v14
	v_cvt_pk_f32_fp8_sdwa v[6:7], v14 src0_sel:WORD_1
	s_waitcnt vmcnt(3)
	v_cvt_pk_f32_fp8_e32 v[50:51], v18
	v_cvt_pk_f32_fp8_sdwa v[52:53], v18 src0_sel:WORD_1
	v_cvt_pk_f32_fp8_e32 v[62:63], v15
	v_cvt_pk_f32_fp8_sdwa v[14:15], v15 src0_sel:WORD_1
	s_waitcnt vmcnt(2)
	v_cvt_pk_f32_fp8_e32 v[54:55], v22
	v_cvt_pk_f32_fp8_sdwa v[56:57], v22 src0_sel:WORD_1
	v_cvt_pk_f32_fp8_e32 v[64:65], v19
	v_cvt_pk_f32_fp8_sdwa v[18:19], v19 src0_sel:WORD_1
	s_waitcnt vmcnt(1)
	v_cvt_pk_f32_fp8_e32 v[58:59], v26
	v_cvt_pk_f32_fp8_sdwa v[60:61], v26 src0_sel:WORD_1
	v_cvt_pk_f32_fp8_e32 v[66:67], v23
	v_cvt_pk_f32_fp8_sdwa v[22:23], v23 src0_sel:WORD_1
	v_cvt_pk_f32_fp8_e32 v[68:69], v27
	v_cvt_pk_f32_fp8_sdwa v[26:27], v27 src0_sel:WORD_1
	v_pk_add_f32 v[4:5], v[4:5], 0 op_sel_hi:[1,0]
	v_pk_add_f32 v[6:7], v[6:7], 0 op_sel_hi:[1,0]
	v_pk_add_f32 v[62:63], v[62:63], 0 op_sel_hi:[1,0]
	v_pk_add_f32 v[14:15], v[14:15], 0 op_sel_hi:[1,0]
	v_pk_add_f32 v[4:5], v[4:5], v[50:51]
	v_pk_add_f32 v[6:7], v[6:7], v[52:53]
	v_cvt_pk_f32_fp8_e32 v[70:71], v16
	v_pk_add_f32 v[50:51], v[62:63], v[64:65]
	v_pk_add_f32 v[14:15], v[14:15], v[18:19]
	v_pk_add_f32 v[4:5], v[4:5], v[54:55]
	v_pk_add_f32 v[6:7], v[6:7], v[56:57]
	v_cvt_pk_f32_fp8_e32 v[74:75], v20
	v_pk_add_f32 v[18:19], v[50:51], v[66:67]
	v_pk_add_f32 v[14:15], v[14:15], v[22:23]
	v_pk_add_f32 v[4:5], v[4:5], v[58:59]
	v_pk_add_f32 v[6:7], v[6:7], v[60:61]
	v_cvt_pk_f32_fp8_e32 v[78:79], v24
	v_pk_add_f32 v[18:19], v[18:19], v[68:69]
	v_pk_add_f32 v[14:15], v[14:15], v[26:27]
	v_pk_fma_f32 v[4:5], v[4:5], s[10:11], v[34:35] op_sel_hi:[1,0,1]
	v_pk_fma_f32 v[6:7], v[6:7], s[10:11], v[36:37] op_sel_hi:[1,0,1]
	v_cvt_pk_f32_fp8_sdwa v[72:73], v16 src0_sel:WORD_1
	v_pk_fma_f32 v[34:35], v[18:19], s[10:11], v[46:47] op_sel_hi:[1,0,1]
	v_pk_fma_f32 v[36:37], v[14:15], s[10:11], v[48:49] op_sel_hi:[1,0,1]
	global_store_dwordx4 v[12:13], v[4:7], off offset:-4096
	global_store_dwordx4 v[12:13], v[34:37], off offset:-4080
	v_cvt_pk_f32_fp8_sdwa v[76:77], v20 src0_sel:WORD_1
	v_cvt_pk_f32_fp8_e32 v[4:5], v28
	v_pk_add_f32 v[18:19], v[70:71], 0 op_sel_hi:[1,0]
	v_cvt_pk_f32_fp8_sdwa v[80:81], v24 src0_sel:WORD_1
	v_pk_add_f32 v[18:19], v[18:19], v[74:75]
	v_cvt_pk_f32_fp8_sdwa v[6:7], v28 src0_sel:WORD_1
	v_pk_add_f32 v[18:19], v[18:19], v[78:79]
	s_waitcnt vmcnt(2)
	v_lshlrev_b32_e32 v14, 16, v30
	v_pk_add_f32 v[4:5], v[18:19], v[4:5]
	v_pk_add_f32 v[18:19], v[72:73], 0 op_sel_hi:[1,0]
	v_and_b32_e32 v15, 0xffff0000, v30
	v_pk_add_f32 v[18:19], v[18:19], v[76:77]
	v_pk_fma_f32 v[4:5], v[4:5], s[10:11], v[14:15] op_sel_hi:[1,0,1]
	v_pk_add_f32 v[18:19], v[18:19], v[80:81]
	v_lshlrev_b32_e32 v14, 16, v31
	v_and_b32_e32 v15, 0xffff0000, v31
	v_pk_add_f32 v[6:7], v[18:19], v[6:7]
	v_cvt_pk_f32_fp8_e32 v[18:19], v25
	v_pk_fma_f32 v[6:7], v[6:7], s[10:11], v[14:15] op_sel_hi:[1,0,1]
	global_store_dwordx4 v[12:13], v[4:7], off offset:-4064
	v_cvt_pk_f32_fp8_e32 v[14:15], v21
	v_cvt_pk_f32_fp8_e32 v[22:23], v29
	v_cvt_pk_f32_fp8_e32 v[4:5], v17
	v_cvt_pk_f32_fp8_sdwa v[6:7], v17 src0_sel:WORD_1
	v_cvt_pk_f32_fp8_sdwa v[16:17], v21 src0_sel:WORD_1
	v_cvt_pk_f32_fp8_sdwa v[20:21], v25 src0_sel:WORD_1
	v_cvt_pk_f32_fp8_sdwa v[24:25], v29 src0_sel:WORD_1
	v_pk_add_f32 v[4:5], v[4:5], 0 op_sel_hi:[1,0]
	v_pk_add_f32 v[6:7], v[6:7], 0 op_sel_hi:[1,0]
	v_pk_add_f32 v[4:5], v[4:5], v[14:15]
	v_pk_add_f32 v[6:7], v[6:7], v[16:17]
	v_pk_add_f32 v[4:5], v[4:5], v[18:19]
	v_pk_add_f32 v[6:7], v[6:7], v[20:21]
	v_lshlrev_b32_e32 v26, 16, v32
	v_and_b32_e32 v27, 0xffff0000, v32
	v_pk_add_f32 v[4:5], v[4:5], v[22:23]
	v_lshlrev_b32_e32 v14, 16, v33
	v_and_b32_e32 v15, 0xffff0000, v33
	v_pk_add_f32 v[6:7], v[6:7], v[24:25]
	v_pk_fma_f32 v[4:5], v[4:5], s[10:11], v[26:27] op_sel_hi:[1,0,1]
	v_pk_fma_f32 v[6:7], v[6:7], s[10:11], v[14:15] op_sel_hi:[1,0,1]
	global_store_dwordx4 v[12:13], v[4:7], off offset:-4048
	global_load_dwordx4 v[4:7], v[38:39], off offset:1024
	s_nop 0
	global_load_dwordx4 v[14:17], v[40:41], off offset:1024
	global_load_dwordx4 v[18:21], v[42:43], off offset:1024
	global_load_dwordx4 v[22:25], v[44:45], off offset:1024
	global_load_dwordx4 v[26:29], v[10:11], off offset:2048
	global_load_dwordx4 v[30:33], v[10:11], off offset:2064
	v_lshl_add_u64 v[10:11], v[10:11], 0, s[12:13]
	s_waitcnt vmcnt(5)
; __device__ __forceinline__ void unpack8(const v4u q, float (&d)[8]) { d[0] = bflo(q.x); d[1] = bfhi(q.x); d[2] = bflo(q.y); d[3] = bfhi(q.y); d[4] = bflo(q.z); d[5] = bfhi(q.z); d[6] = bflo(q.w); d[7] = bfhi(q.w); }
; __device__ __forceinline__ void phase_combine(const Params& p, const LAS int* tstart, int gw, int NGW, int lane) {
;     ...
;     for (int m = gw; m < T; m += NGW) {
;         const i32x4v ce = ne, cp = np;
;         if (m + NGW < T) { ne = *(const i32x4v*)(toke + (m + NGW) * 4); np = *(const i32x4v*)(tokp + (m + NGW) * 4); }
;     ...
;         for (int j = 0; j < 2; ++j) { const int c = (j * 64 + lane) * 16;
;             v4u w[4];
; #pragma unroll
;             for (int k = 0; k < 4; ++k) w[k] = *(const v4u*)(yr[k] + c);
;             f32x4 a[4];
;             { const v4u xa = *(const v4u*)(xp + c), xb = *(const v4u*)(xp + c + 8); float fa[8], fb[8]; unpack8(xa, fa); unpack8(xb, fb);
;               a[0] = (f32x4){fa[0], fa[1], fa[2], fa[3]}; a[1] = (f32x4){fa[4], fa[5], fa[6], fa[7]}; a[2] = (f32x4){fb[0], fb[1], fb[2], fb[3]}; a[3] = (f32x4){fb[4], fb[5], fb[6], fb[7]}; }
; #pragma unroll
;             for (int q = 0; q < 4; ++q) { float s0 = 0.f, s1 = 0.f, s2 = 0.f, s3 = 0.f;
; #pragma unroll
;                 for (int k = 0; k < 4; ++k) { const int wd = (int)(q == 0 ? w[k].x : q == 1 ? w[k].y : q == 2 ? w[k].z : w[k].w);
;                     const f32x2 lo = __builtin_amdgcn_cvt_pk_f32_fp8(wd, false), hi = __builtin_amdgcn_cvt_pk_f32_fp8(wd, true);
;                     s0 += lo.x; s1 += lo.y; s2 += hi.x; s3 += hi.y; }
;                 a[q][0] += s0 * DY; a[q][1] += s1 * DY; a[q][2] += s2 * DY; a[q][3] += s3 * DY;
;                 *(f32x4*)(op + c + 4 * q) = a[q]; }
	v_cvt_pk_f32_fp8_e32 v[34:35], v4
	v_cvt_pk_f32_fp8_sdwa v[36:37], v4 src0_sel:WORD_1
	s_waitcnt vmcnt(4)
	v_cvt_pk_f32_fp8_e32 v[38:39], v14
	v_cvt_pk_f32_fp8_sdwa v[40:41], v14 src0_sel:WORD_1
	s_waitcnt vmcnt(1)
	v_lshlrev_b32_e32 v50, 16, v26
	v_and_b32_e32 v51, 0xffff0000, v26
	v_lshlrev_b32_e32 v52, 16, v27
	v_and_b32_e32 v53, 0xffff0000, v27
	v_cvt_pk_f32_fp8_e32 v[26:27], v5
	v_cvt_pk_f32_fp8_sdwa v[4:5], v5 src0_sel:WORD_1
	v_cvt_pk_f32_fp8_e32 v[54:55], v15
	v_cvt_pk_f32_fp8_sdwa v[14:15], v15 src0_sel:WORD_1
	v_cvt_pk_f32_fp8_e32 v[42:43], v18
	v_cvt_pk_f32_fp8_sdwa v[44:45], v18 src0_sel:WORD_1
	v_cvt_pk_f32_fp8_e32 v[56:57], v19
	v_cvt_pk_f32_fp8_sdwa v[18:19], v19 src0_sel:WORD_1
	v_cvt_pk_f32_fp8_e32 v[46:47], v22
	v_cvt_pk_f32_fp8_sdwa v[48:49], v22 src0_sel:WORD_1
	v_cvt_pk_f32_fp8_e32 v[58:59], v23
	v_cvt_pk_f32_fp8_sdwa v[22:23], v23 src0_sel:WORD_1
	v_pk_add_f32 v[4:5], v[4:5], 0 op_sel_hi:[1,0]
	v_lshlrev_b32_e32 v60, 16, v28
	v_and_b32_e32 v61, 0xffff0000, v28
	v_lshlrev_b32_e32 v62, 16, v29
	v_and_b32_e32 v63, 0xffff0000, v29
	v_pk_add_f32 v[28:29], v[34:35], 0 op_sel_hi:[1,0]
	v_pk_add_f32 v[34:35], v[36:37], 0 op_sel_hi:[1,0]
	v_pk_add_f32 v[4:5], v[4:5], v[14:15]
	v_pk_add_f32 v[26:27], v[26:27], 0 op_sel_hi:[1,0]
	v_pk_add_f32 v[28:29], v[28:29], v[38:39]
	v_pk_add_f32 v[34:35], v[34:35], v[40:41]
	v_pk_add_f32 v[4:5], v[4:5], v[18:19]
	v_pk_add_f32 v[26:27], v[26:27], v[54:55]
	v_pk_add_f32 v[14:15], v[28:29], v[42:43]
	v_pk_add_f32 v[28:29], v[34:35], v[44:45]
	v_pk_add_f32 v[4:5], v[4:5], v[22:23]
	v_pk_add_f32 v[26:27], v[26:27], v[56:57]
	v_pk_add_f32 v[14:15], v[14:15], v[46:47]
	v_pk_add_f32 v[18:19], v[28:29], v[48:49]
	v_pk_fma_f32 v[36:37], v[4:5], s[10:11], v[62:63] op_sel_hi:[1,0,1]
	v_cvt_pk_f32_fp8_e32 v[4:5], v6
	v_pk_add_f32 v[34:35], v[26:27], v[58:59]
	v_pk_fma_f32 v[26:27], v[14:15], s[10:11], v[50:51] op_sel_hi:[1,0,1]
	v_pk_fma_f32 v[28:29], v[18:19], s[10:11], v[52:53] op_sel_hi:[1,0,1]
	v_cvt_pk_f32_fp8_sdwa v[14:15], v6 src0_sel:WORD_1
	v_cvt_pk_f32_fp8_e32 v[18:19], v16
	v_pk_fma_f32 v[34:35], v[34:35], s[10:11], v[60:61] op_sel_hi:[1,0,1]
	global_store_dwordx4 v[12:13], v[26:29], off
	v_cvt_pk_f32_fp8_sdwa v[22:23], v16 src0_sel:WORD_1
	global_store_dwordx4 v[12:13], v[34:37], off offset:16
	v_cvt_pk_f32_fp8_e32 v[26:27], v20
	v_cvt_pk_f32_fp8_sdwa v[28:29], v20 src0_sel:WORD_1
	v_cvt_pk_f32_fp8_e32 v[34:35], v24
	v_cvt_pk_f32_fp8_sdwa v[36:37], v24 src0_sel:WORD_1
	v_pk_add_f32 v[4:5], v[4:5], 0 op_sel_hi:[1,0]
	v_pk_add_f32 v[14:15], v[14:15], 0 op_sel_hi:[1,0]
	v_pk_add_f32 v[4:5], v[4:5], v[18:19]
	v_pk_add_f32 v[14:15], v[14:15], v[22:23]
	v_pk_add_f32 v[4:5], v[4:5], v[26:27]
	s_waitcnt vmcnt(2)
	v_lshlrev_b32_e32 v38, 16, v30
	v_and_b32_e32 v39, 0xffff0000, v30
	v_pk_add_f32 v[4:5], v[4:5], v[34:35]
	v_pk_add_f32 v[14:15], v[14:15], v[28:29]
	v_pk_fma_f32 v[26:27], v[4:5], s[10:11], v[38:39] op_sel_hi:[1,0,1]
	v_lshlrev_b32_e32 v4, 16, v31
	v_and_b32_e32 v5, 0xffff0000, v31
	v_pk_add_f32 v[14:15], v[14:15], v[36:37]
	v_cvt_pk_f32_fp8_e32 v[18:19], v21
	v_pk_fma_f32 v[28:29], v[14:15], s[10:11], v[4:5] op_sel_hi:[1,0,1]
	v_cvt_pk_f32_fp8_e32 v[4:5], v7
	v_cvt_pk_f32_fp8_sdwa v[6:7], v7 src0_sel:WORD_1
	v_cvt_pk_f32_fp8_e32 v[14:15], v17
	v_cvt_pk_f32_fp8_sdwa v[16:17], v17 src0_sel:WORD_1
	v_cvt_pk_f32_fp8_sdwa v[20:21], v21 src0_sel:WORD_1
	v_cvt_pk_f32_fp8_e32 v[22:23], v25
	v_cvt_pk_f32_fp8_sdwa v[24:25], v25 src0_sel:WORD_1
	v_pk_add_f32 v[4:5], v[4:5], 0 op_sel_hi:[1,0]
	v_pk_add_f32 v[6:7], v[6:7], 0 op_sel_hi:[1,0]
	v_pk_add_f32 v[4:5], v[4:5], v[14:15]
	v_pk_add_f32 v[6:7], v[6:7], v[16:17]
	v_pk_add_f32 v[4:5], v[4:5], v[18:19]
	v_pk_add_f32 v[6:7], v[6:7], v[20:21]
	global_store_dwordx4 v[12:13], v[26:29], off offset:32
	v_pk_add_f32 v[4:5], v[4:5], v[22:23]
	v_lshlrev_b32_e32 v14, 16, v33
	v_lshlrev_b32_e32 v26, 16, v32
	v_and_b32_e32 v27, 0xffff0000, v32
	v_and_b32_e32 v15, 0xffff0000, v33
	v_pk_add_f32 v[6:7], v[6:7], v[24:25]
	v_pk_fma_f32 v[4:5], v[4:5], s[10:11], v[26:27] op_sel_hi:[1,0,1]
	v_pk_fma_f32 v[6:7], v[6:7], s[10:11], v[14:15] op_sel_hi:[1,0,1]
	global_store_dwordx4 v[12:13], v[4:7], off offset:48
	v_lshl_add_u64 v[12:13], v[12:13], 0, s[14:15]
	s_nop 0
	v_mov_b64_e32 v[6:7], v[2:3]
	v_mov_b64_e32 v[4:5], v[0:1]
	s_cbranch_vccz .LBB0_874
.LBB0_872:
	s_add_i32 s90, s90, s68
	s_cmpk_gt_i32 s90, 0x7fff
	s_cselect_b64 s[18:19], -1, 0
	s_and_b64 vcc, exec, s[18:19]
	s_cbranch_vccnz .LBB0_871
	s_ashr_i32 s17, s16, 31
	s_lshl_b64 s[0:1], s[16:17], 2
	s_add_u32 s2, s11, s0
	s_addc_u32 s3, s20, s1
	s_add_u32 s0, s21, s0
	s_addc_u32 s1, s22, s1
	global_load_dwordx4 v[84:87], v9, s[0:1]
	global_load_dwordx4 v[0:3], v9, s[2:3]
	s_branch .LBB0_871
